# v41 + final phase: next row's tok_e/tok_rank pairs loaded ahead of the current row's 8 output stores; loop-top wait vmcnt(8) (stores stay in flight, tok latency hidden)
# speedup vs baseline: 1.0031x; 1.0031x over previous
; #define GAS __attribute__((address_space(1)))
; __device__ __forceinline__ void final_phase(Frame& F) {
;     const bf16* Y2 = WSP(const bf16, WS_Z); const float* mod = WSP(const float, WS_MOD1); const float* fg = F.in[34];
;     const int* tok_e = WSP(const int, WS_ROUTE); const int* tok_rank = tok_e + 2 * ML; const float* tok_w = (const float*)(tok_rank + 2 * ML);
;     int off[8]; { int t = 0;
; #pragma unroll
;         for (int e = 0; e < 8; ++e) { off[e] = t; t += ((__builtin_amdgcn_readfirstlane((int)F.ctl[CW_CNT + e]) + 255) >> 8) << 8; } }
;     const int gw = F.vcu * NWAVES + F.wave, NGW = F.G * NWAVES;
;     for (int row = gw; row < ML; row += NGW) {
;         const int e0 = tok_e[2 * row], e1 = tok_e[2 * row + 1]; int o0 = 0, o1 = 0;
; #pragma unroll
;         for (int k = 0; k < 8; ++k) { o0 = (e0 == k) ? off[k] : o0; o1 = (e1 == k) ? off[k] : o1; }
;         const size_t s0 = (size_t)(o0 + tok_rank[2 * row]) * DM, s1 = (size_t)(o1 + tok_rank[2 * row + 1]) * DM; const float w0 = tok_w[2 * row], w1 = tok_w[2 * row + 1];
;         const float* g2 = mod + (size_t)(row >> 13) * MOD_W + 5 * DM;
;         GAS f32x4* xr = (GAS f32x4*)(F.out + (size_t)row * DM) + F.lane;
.LBB0_2186:
	s_cmp_lt_i32 s90, 20
	s_cselect_b64 s[2:3], -1, 0
	s_and_b64 s[0:1], s[2:3], s[0:1]
	s_andn2_b64 vcc, exec, s[0:1]
	s_cbranch_vccnz .LBB0_2258
	s_add_u32 s0, s88, 0x8000
	v_mov_b32_e32 v0, 0x8000
	s_waitcnt vmcnt(0)
	v_mov_b32_e32 v29, 0
	s_addc_u32 s1, s89, 0
	global_load_dwordx4 v[0:3], v0, s[88:89]
	s_nop 0
	global_load_dwordx3 v[4:6], v29, s[0:1] offset:16
	s_lshl_b32 s0, s92, 3
	s_add_i32 s6, s0, s94
	s_cmpk_gt_i32 s6, 0x3fff
	s_waitcnt vmcnt(0)
	v_readfirstlane_b32 s7, v0
	v_readfirstlane_b32 s5, v1
	v_readfirstlane_b32 s4, v2
	v_readfirstlane_b32 s3, v3
	v_readfirstlane_b32 s2, v4
	v_readfirstlane_b32 s1, v5
	v_readfirstlane_b32 s0, v6
	s_cbranch_scc1 .LBB0_2258
	v_mbcnt_lo_u32_b32 v0, -1, 0
	v_mbcnt_hi_u32_b32 v0, -1, v0
	v_and_b32_e32 v1, 64, v0
	v_add_u32_e32 v1, 64, v1
	v_xor_b32_e32 v2, 1, v0
	v_cmp_lt_i32_e32 vcc, v2, v1
	s_add_u32 s28, s88, 0x220000
	s_addc_u32 s29, s89, 0
	v_cndmask_b32_e32 v2, v0, v2, vcc
	s_addk_i32 s7, 0xff
	s_addk_i32 s5, 0xff
	v_lshlrev_b32_e32 v31, 2, v2
	v_xor_b32_e32 v2, 2, v0
	s_and_b32 s30, s7, 0xffffff00
	s_and_b32 s31, s5, 0xffffff00
	s_addk_i32 s4, 0xff
	v_cmp_lt_i32_e32 vcc, v2, v1
	s_add_i32 s31, s31, s30
	s_and_b32 s33, s4, 0xffffff00
	s_addk_i32 s3, 0xff
	v_cndmask_b32_e32 v2, v0, v2, vcc
	s_add_i32 s33, s33, s31
	s_and_b32 s34, s3, 0xffffff00
	s_addk_i32 s2, 0xff
	s_waitcnt lgkmcnt(0)
	v_lshlrev_b32_e32 v35, 2, v2
	v_xor_b32_e32 v2, 4, v0
	s_add_i32 s34, s34, s33
	s_and_b32 s35, s2, 0xffffff00
	s_addk_i32 s1, 0xff
	v_cmp_lt_i32_e32 vcc, v2, v1
	s_add_i32 s35, s35, s34
	s_and_b32 s36, s1, 0xffffff00
	s_addk_i32 s0, 0xff
	v_cndmask_b32_e32 v2, v0, v2, vcc
	s_add_i32 s36, s36, s35
	s_and_b32 s37, s0, 0xffffff00
	v_lshlrev_b32_e32 v37, 2, v2
	v_xor_b32_e32 v2, 8, v0
	s_add_i32 s37, s37, s36
	v_cmp_lt_i32_e32 vcc, v2, v1
	s_add_u32 s8, s88, 0x26700000
	s_addc_u32 s9, s89, 0
	v_cndmask_b32_e32 v2, v0, v2, vcc
	v_lshlrev_b32_e32 v39, 2, v2
	v_xor_b32_e32 v2, 16, v0
	s_add_u32 s38, s88, 0x200000
	v_cmp_lt_i32_e32 vcc, v2, v1
	s_addc_u32 s39, s89, 0
	s_add_u32 s40, s88, 0x240000
	v_cndmask_b32_e32 v2, v0, v2, vcc
	v_lshlrev_b32_e32 v41, 2, v2
	v_xor_b32_e32 v2, 32, v0
	s_addc_u32 s41, s89, 0
	s_lshl_b32 s10, s93, 3
	v_cmp_lt_i32_e32 vcc, v2, v1
	v_lshlrev_b32_e32 v30, 2, v178
	v_readlane_b32 s12, v250, 0
	v_cndmask_b32_e32 v0, v0, v2, vcc
	v_readlane_b32 s13, v250, 1
	v_readlane_b32 s14, v250, 2
	v_readlane_b32 s15, v250, 3
	v_readlane_b32 s16, v250, 4
	v_readlane_b32 s17, v250, 5
	v_or_b32_e32 v44, 0x500, v30
	s_add_u32 s42, s88, 0x15a00000
	v_lshlrev_b32_e32 v45, 2, v0
	v_readlane_b32 s18, v250, 6
	v_readlane_b32 s19, v250, 7
	s_mov_b64 s[12:13], s[16:17]
	v_lshlrev_b32_e32 v0, 2, v44
	v_mov_b32_e32 v1, v29
	v_or_b32_e32 v48, 0x600, v30
	s_addc_u32 s43, s89, 0
	s_ashr_i32 s7, s6, 31
	v_lshl_add_u64 v[46:47], s[12:13], 0, v[0:1]
	v_lshlrev_b32_e32 v0, 2, v48
	v_or_b32_e32 v52, 0x700, v30
	s_lshl_b64 s[2:3], s[6:7], 12
	v_lshl_add_u64 v[50:51], s[12:13], 0, v[0:1]
	v_lshlrev_b32_e32 v0, 2, v52
	s_add_u32 s2, s88, s2
	v_lshl_add_u64 v[54:55], s[12:13], 0, v[0:1]
	v_lshlrev_b32_e32 v0, 3, v178
	s_addc_u32 s3, s89, s3
	v_lshlrev_b32_e32 v28, 4, v178
	v_lshl_add_u64 v[56:57], s[8:9], 0, v[0:1]
	v_lshl_add_u64 v[0:1], s[2:3], 0, v[0:1]
	s_mov_b64 s[2:3], 0x4d800000
	s_ashr_i32 s11, s10, 31
	s_mov_b64 s[14:15], s[18:19]
	v_lshl_add_u64 v[32:33], s[12:13], 0, v[28:29]
	v_lshl_add_u64 v[58:59], v[0:1], 0, s[2:3]
	s_lshl_b64 s[12:13], s[10:11], 12
	s_lshl_b64 s[2:3], s[6:7], 13
	s_add_u32 s2, s14, s2
	s_addc_u32 s3, s15, s3
	s_mov_b64 s[0:1], 0x1000
	v_lshl_add_u64 v[0:1], s[2:3], 0, v[28:29]
	v_lshl_add_u64 v[42:43], v[32:33], 0, s[0:1]
	v_lshl_add_u64 v[60:61], v[0:1], 0, s[0:1]
	s_lshl_b32 s0, s92, 4
	s_lshl_b32 s1, s94, 1
	v_or_b32_e32 v34, 0x100, v30
	v_or_b32_e32 v36, 0x200, v30
	v_or_b32_e32 v38, 0x300, v30
	v_or_b32_e32 v40, 0x400, v30
	s_lshl_b64 s[14:15], s[10:11], 13
	s_add_i32 s16, s0, s1
	s_lshl_b32 s7, s93, 4
	v_mov_b32_e32 v49, 0x358637bd
	s_mov_b32 s11, 0xf800000
	v_mov_b32_e32 v53, 0x260
	v_mov_b64_e32 v[62:63], 0x3ffffff
	s_mov_b32 s98, s16
	s_ashr_i32 s99, s16, 31
	s_lshl_b64 s[98:99], s[98:99], 2
	s_add_u32 s100, s38, s98
	s_addc_u32 s101, s39, s99
	global_load_dwordx2 v[232:233], v29, s[100:101]
	s_add_u32 s100, s28, s98
	s_addc_u32 s101, s29, s99
	global_load_dwordx2 v[234:235], v29, s[100:101]
	global_load_dwordx4 v[200:203], v[32:33], off
	global_load_dwordx4 v[204:207], v[32:33], off offset:1024
	global_load_dwordx4 v[208:211], v[32:33], off offset:2048
	global_load_dwordx4 v[212:215], v[32:33], off offset:3072
	global_load_dwordx4 v[216:219], v[42:43], off
	global_load_dwordx4 v[220:223], v[46:47], off
	global_load_dwordx4 v[224:227], v[50:51], off
	global_load_dwordx4 v[228:231], v[54:55], off
	s_branch .LBB0_2191

; #define GAS __attribute__((address_space(1)))
; __device__ __forceinline__ void final_phase(Frame& F) {
;     ...
;                 const v2u ya = *(const GAS v2u*)(Y2 + s0 + col), yb = *(const GAS v2u*)(Y2 + s1 + col); const f32x4 gg = *(const GAS f32x4*)(g2 + col);
;                 f32x4 mo; mo.x = w0 * bflo(ya.x) + w1 * bflo(yb.x); mo.y = w0 * bfhi(ya.x) + w1 * bfhi(yb.x); mo.z = w0 * bflo(ya.y) + w1 * bflo(yb.y); mo.w = w0 * bfhi(ya.y) + w1 * bfhi(yb.y);
;                 { const v2u hw = hr[64 * j]; f32x4 hv; hv.x = bflo(hw.x); hv.y = bfhi(hw.x); hv.z = bflo(hw.y); hv.w = bfhi(hw.y); v[j] = hv + gg * mo; } s += (v[j].x * v[j].x + v[j].y * v[j].y) + (v[j].z * v[j].z + v[j].w * v[j].w); }
;         } else {
; #pragma unroll
;             for (int j = 0; j < 8; ++j) { const int col = 4 * (F.lane + 64 * j);
;                 const f32x4 fa = y2_load(F, Y2, s0, col), fb = y2_load(F, Y2, s1, col); const f32x4 gg = *(const GAS f32x4*)(g2 + col);
;                 const f32x4 mo = w0 * fa + w1 * fb;
;                 { const v2u hw = hr[64 * j]; f32x4 hv; hv.x = bflo(hw.x); hv.y = bfhi(hw.x); hv.z = bflo(hw.y); hv.w = bfhi(hw.y); v[j] = hv + gg * mo; } s += (v[j].x * v[j].x + v[j].y * v[j].y) + (v[j].z * v[j].z + v[j].w * v[j].w); }
;         }
;         const float rstd = 1.0f / sqrtf(wave_sum(s) * (1.0f / DM) + NORM_EPS);
; #pragma unroll
;         for (int j = 0; j < 8; ++j) { const int col = 4 * (F.lane + 64 * j); xr[64 * j] = v[j] * rstd * *(const GAS f32x4*)(fg + col); }
.LBB0_2190:
	s_waitcnt vmcnt(2)
	v_mul_f32_e32 v64, v5, v5
	v_mul_f32_e32 v65, v7, v7
	v_fmac_f32_e32 v64, v4, v4
	v_fmac_f32_e32 v65, v6, v6
	v_add_f32_e32 v64, v64, v65
	v_add_f32_e32 v28, v28, v64
	ds_bpermute_b32 v64, v31, v28
	s_add_i32 s6, s6, s10
	s_add_i32 s16, s16, s7
	s_mov_b32 s98, s16
	s_ashr_i32 s99, s16, 31
	s_lshl_b64 s[98:99], s[98:99], 2
	s_add_u32 s100, s38, s98
	s_addc_u32 s101, s39, s99
	global_load_dwordx2 v[232:233], v29, s[100:101]
	s_add_u32 s100, s28, s98
	s_addc_u32 s101, s29, s99
	global_load_dwordx2 v[234:235], v29, s[100:101]
	v_lshl_add_u64 v[58:59], v[58:59], 0, s[12:13]
	s_cmpk_lt_i32 s6, 0x4000
	s_waitcnt lgkmcnt(0)
	v_add_f32_e32 v28, v28, v64
	ds_bpermute_b32 v64, v35, v28
	s_waitcnt lgkmcnt(0)
	v_add_f32_e32 v28, v28, v64
	ds_bpermute_b32 v64, v37, v28
	s_waitcnt lgkmcnt(0)
	v_add_f32_e32 v28, v28, v64
	ds_bpermute_b32 v64, v39, v28
	s_waitcnt lgkmcnt(0)
	v_add_f32_e32 v28, v28, v64
	ds_bpermute_b32 v64, v41, v28
	s_waitcnt lgkmcnt(0)
	v_add_f32_e32 v28, v28, v64
	ds_bpermute_b32 v64, v45, v28
	s_waitcnt lgkmcnt(0)
	v_add_f32_e32 v28, v28, v64
	v_fmamk_f32 v28, v28, 0x3a000000, v49
	v_mul_f32_e32 v64, 0x4f800000, v28
	v_cmp_gt_f32_e32 vcc, s11, v28
	s_nop 1
	v_cndmask_b32_e32 v28, v28, v64, vcc
	v_sqrt_f32_e32 v64, v28
	s_nop 0
	v_add_u32_e32 v65, -1, v64
	s_waitcnt vmcnt(1)
	v_add_u32_e32 v66, 1, v64
	v_fma_f32 v67, -v65, v64, v28
	v_fma_f32 v76, -v66, v64, v28
	v_cmp_ge_f32_e64 s[0:1], 0, v67
	s_nop 1
	v_cndmask_b32_e64 v64, v64, v65, s[0:1]
	v_cmp_lt_f32_e64 s[0:1], 0, v76
	s_nop 1
	v_cndmask_b32_e64 v64, v64, v66, s[0:1]
	v_mul_f32_e32 v65, 0x37800000, v64
	v_cndmask_b32_e32 v64, v64, v65, vcc
	v_cmp_class_f32_e32 vcc, v28, v53
	s_nop 1
	v_cndmask_b32_e32 v28, v64, v28, vcc
	v_div_scale_f32 v64, s[0:1], v28, v28, 1.0
	v_rcp_f32_e32 v65, v64
	v_div_scale_f32 v66, vcc, 1.0, v28, 1.0
	v_fma_f32 v67, -v64, v65, 1.0
	v_fmac_f32_e32 v65, v67, v65
	v_mul_f32_e32 v67, v66, v65
	v_fma_f32 v76, -v64, v67, v66
	v_fmac_f32_e32 v67, v76, v65
	v_fma_f32 v64, -v64, v67, v66
	v_div_fmas_f32 v64, v64, v65, v67
	v_div_fixup_f32 v28, v64, v28, 1.0
	v_pk_mul_f32 v[64:65], v[70:71], v[28:29] op_sel_hi:[1,0]
	v_pk_mul_f32 v[66:67], v[68:69], v[28:29] op_sel_hi:[1,0]
	s_waitcnt vmcnt(0)
	v_pk_mul_f32 v[24:25], v[200:201], v[64:65]
	v_pk_mul_f32 v[26:27], v[202:203], v[66:67]
	global_store_dwordx4 v[60:61], v[24:27], off offset:-4096
	s_nop 1
	v_pk_mul_f32 v[64:65], v[72:73], v[28:29] op_sel_hi:[1,0]
	v_pk_mul_f32 v[66:67], v[74:75], v[28:29] op_sel_hi:[1,0]
	v_pk_mul_f32 v[10:11], v[10:11], v[28:29] op_sel_hi:[1,0]
	v_pk_mul_f32 v[8:9], v[8:9], v[28:29] op_sel_hi:[1,0]
	v_pk_mul_f32 v[14:15], v[14:15], v[28:29] op_sel_hi:[1,0]
	v_pk_mul_f32 v[12:13], v[12:13], v[28:29] op_sel_hi:[1,0]
	v_pk_mul_f32 v[2:3], v[2:3], v[28:29] op_sel_hi:[1,0]
	v_pk_mul_f32 v[0:1], v[0:1], v[28:29] op_sel_hi:[1,0]
	v_pk_mul_f32 v[6:7], v[6:7], v[28:29] op_sel_hi:[1,0]
	v_pk_mul_f32 v[4:5], v[4:5], v[28:29] op_sel_hi:[1,0]
	v_pk_mul_f32 v[24:25], v[204:205], v[66:67]
	v_pk_mul_f32 v[26:27], v[206:207], v[64:65]
	global_store_dwordx4 v[60:61], v[24:27], off offset:-3072
	s_nop 1
	v_pk_mul_f32 v[8:9], v[208:209], v[8:9]
	v_pk_mul_f32 v[10:11], v[210:211], v[10:11]
	global_store_dwordx4 v[60:61], v[8:11], off offset:-2048
	s_nop 1
	v_pk_mul_f32 v[8:9], v[212:213], v[12:13]
	v_pk_mul_f32 v[10:11], v[214:215], v[14:15]
	global_store_dwordx4 v[60:61], v[8:11], off offset:-1024
	s_nop 1
	v_pk_mul_f32 v[12:13], v[18:19], v[28:29] op_sel_hi:[1,0]
	v_pk_mul_f32 v[14:15], v[16:17], v[28:29] op_sel_hi:[1,0]
	v_pk_mul_f32 v[10:11], v[12:13], v[218:219]
	v_pk_mul_f32 v[8:9], v[14:15], v[216:217]
	global_store_dwordx4 v[60:61], v[8:11], off
	s_nop 1
	v_pk_mul_f32 v[12:13], v[22:23], v[28:29] op_sel_hi:[1,0]
	v_pk_mul_f32 v[14:15], v[20:21], v[28:29] op_sel_hi:[1,0]
	v_pk_mul_f32 v[10:11], v[12:13], v[222:223]
	v_pk_mul_f32 v[8:9], v[14:15], v[220:221]
	global_store_dwordx4 v[60:61], v[8:11], off offset:1024
	s_nop 1
	v_pk_mul_f32 v[0:1], v[0:1], v[224:225]
	v_pk_mul_f32 v[2:3], v[2:3], v[226:227]
	global_store_dwordx4 v[60:61], v[0:3], off offset:2048
	s_nop 1
	v_pk_mul_f32 v[0:1], v[4:5], v[228:229]
	v_pk_mul_f32 v[2:3], v[6:7], v[230:231]
	global_store_dwordx4 v[60:61], v[0:3], off offset:3072
	s_nop 1
	v_lshl_add_u64 v[60:61], v[60:61], 0, s[14:15]
	s_cbranch_scc0 .LBB0_2258
; #define GAS __attribute__((address_space(1)))
; __device__ __forceinline__ void final_phase(Frame& F) {
;     ...
;     for (int row = gw; row < ML; row += NGW) {
;         const int e0 = tok_e[2 * row], e1 = tok_e[2 * row + 1]; int o0 = 0, o1 = 0;
; #pragma unroll
;         for (int k = 0; k < 8; ++k) { o0 = (e0 == k) ? off[k] : o0; o1 = (e1 == k) ? off[k] : o1; }
;         const size_t s0 = (size_t)(o0 + tok_rank[2 * row]) * DM, s1 = (size_t)(o1 + tok_rank[2 * row + 1]) * DM; const float w0 = tok_w[2 * row], w1 = tok_w[2 * row + 1];
;         const float* g2 = mod + (size_t)(row >> 13) * MOD_W + 5 * DM;
;         GAS f32x4* xr = (GAS f32x4*)(F.out + (size_t)row * DM) + F.lane;
;         const GAS v2u* hr = (const GAS v2u*)(WSP(const bf16, WS_H) + (size_t)row * DM) + F.lane;
;         f32x4 v[8]; float s = 0.f;
;         const bool tail = __builtin_amdgcn_readfirstlane((int)((s0 >= (size_t)Y2_FULL_TILES * 256 * DM) | (s1 >= (size_t)Y2_FULL_TILES * 256 * DM))) != 0;
;         if (!tail) {
; #pragma unroll
;             for (int j = 0; j < 8; ++j) { const int col = 4 * (F.lane + 64 * j);
;                 const v2u ya = *(const GAS v2u*)(Y2 + s0 + col), yb = *(const GAS v2u*)(Y2 + s1 + col); const f32x4 gg = *(const GAS f32x4*)(g2 + col);
;                 f32x4 mo; mo.x = w0 * bflo(ya.x) + w1 * bflo(yb.x); mo.y = w0 * bfhi(ya.x) + w1 * bfhi(yb.x); mo.z = w0 * bflo(ya.y) + w1 * bflo(yb.y); mo.w = w0 * bfhi(ya.y) + w1 * bfhi(yb.y);
;                 { const v2u hw = hr[64 * j]; f32x4 hv; hv.x = bflo(hw.x); hv.y = bfhi(hw.x); hv.z = bflo(hw.y); hv.w = bfhi(hw.y); v[j] = hv + gg * mo; } s += (v[j].x * v[j].x + v[j].y * v[j].y) + (v[j].z * v[j].z + v[j].w * v[j].w); }
.LBB0_2191:
	s_ashr_i32 s17, s16, 31
	s_lshl_b64 s[2:3], s[16:17], 2
	s_add_i32 s0, s16, 1
	s_ashr_i32 s1, s0, 31
	v_lshlrev_b32_e32 v78, 2, v30
	v_lshlrev_b32_e32 v88, 2, v34
	v_lshlrev_b32_e32 v67, 2, v36
	v_lshlrev_b32_e32 v27, 2, v38
	v_lshlrev_b32_e32 v26, 2, v40
	v_lshlrev_b32_e32 v25, 2, v44
	v_lshlrev_b32_e32 v24, 2, v48
	v_lshlrev_b32_e32 v65, 2, v52
	s_waitcnt vmcnt(8)
	v_readfirstlane_b32 s4, v232
	v_readfirstlane_b32 s5, v233
	s_cmp_eq_u32 s4, 1
	s_cselect_b32 s17, s30, 0
	s_cmp_eq_u32 s5, 1
	s_cselect_b32 s18, s30, 0
	s_cmp_eq_u32 s4, 2
	s_cselect_b32 s17, s31, s17
	s_cmp_eq_u32 s5, 2
	s_cselect_b32 s18, s31, s18
	s_cmp_eq_u32 s4, 3
	s_cselect_b32 s17, s33, s17
	s_cmp_eq_u32 s5, 3
	s_cselect_b32 s18, s33, s18
	s_cmp_eq_u32 s4, 4
	s_cselect_b32 s17, s34, s17
	s_cmp_eq_u32 s5, 4
	s_cselect_b32 s18, s34, s18
	s_cmp_eq_u32 s4, 5
	s_cselect_b32 s17, s35, s17
	s_cmp_eq_u32 s5, 5
	s_cselect_b32 s18, s35, s18
	s_cmp_eq_u32 s4, 6
	s_cselect_b32 s17, s36, s17
	s_cmp_eq_u32 s5, 6
	s_cselect_b32 s18, s36, s18
	s_cmp_eq_u32 s4, 7
	s_cselect_b32 s17, s37, s17
	s_cmp_eq_u32 s5, 7
	s_cselect_b32 s20, s37, s18
	s_lshl_b64 s[18:19], s[0:1], 2
	v_readfirstlane_b32 s0, v234
	s_add_i32 s0, s17, s0
	s_ashr_i32 s1, s0, 31
	s_lshl_b64 s[4:5], s[0:1], 11
	v_readfirstlane_b32 s0, v235
	s_add_i32 s0, s20, s0
	s_ashr_i32 s1, s0, 31
	s_lshl_b64 s[0:1], s[0:1], 11
	s_add_u32 s2, s40, s2
	s_addc_u32 s3, s41, s3
	s_add_u32 s18, s40, s18
	s_addc_u32 s19, s41, s19
	global_load_dword v64, v29, s[2:3]
	global_load_dword v66, v29, s[18:19]
	s_ashr_i32 s2, s6, 13
	s_mul_hi_i32 s3, s2, 0xc000
	s_mul_i32 s2, s2, 0xc000
	s_add_u32 s2, s88, s2
	s_addc_u32 s3, s89, s3
	s_add_u32 s18, s2, 0x12e000
	s_addc_u32 s19, s3, 0
	s_or_b64 s[2:3], s[0:1], s[4:5]
	v_cmp_gt_u64_e32 vcc, s[2:3], v[62:63]
	s_nop 1
	v_cndmask_b32_e64 v0, 0, 1, vcc
	s_nop 0
	v_readfirstlane_b32 s2, v0
	s_bitcmp1_b32 s2, 0
	s_cselect_b64 s[20:21], -1, 0
	s_mov_b64 s[2:3], -1
	s_and_b64 vcc, exec, s[20:21]
	s_cbranch_vccnz .LBB0_2193
	global_load_dwordx2 v[18:19], v[58:59], off
	global_load_dwordx2 v[68:69], v[58:59], off offset:512
	global_load_dwordx2 v[70:71], v[58:59], off offset:1024
	v_lshl_add_u64 v[6:7], s[4:5], 1, v[56:57]
	global_load_dwordx2 v[72:73], v[6:7], off
	v_lshl_add_u64 v[4:5], s[0:1], 1, v[56:57]
	global_load_dwordx2 v[74:75], v[4:5], off
	global_load_dwordx2 v[76:77], v[6:7], off offset:512
	global_load_dwordx2 v[90:91], v[4:5], off offset:512
	global_load_dwordx2 v[92:93], v[6:7], off offset:1024
	global_load_dwordx2 v[94:95], v[4:5], off offset:1024
	global_load_dwordx4 v[8:11], v78, s[18:19]
	global_load_dwordx4 v[12:15], v88, s[18:19]
	global_load_dwordx4 v[80:83], v67, s[18:19]
	global_load_dwordx2 v[96:97], v[6:7], off offset:1536
	global_load_dwordx2 v[98:99], v[4:5], off offset:1536
	global_load_dwordx4 v[84:87], v27, s[18:19]
	global_load_dwordx2 v[100:101], v[58:59], off offset:1536
	global_load_dwordx4 v[0:3], v26, s[18:19]
	global_load_dwordx2 v[16:17], v[58:59], off offset:2048
	global_load_dwordx2 v[102:103], v[6:7], off offset:2048
	global_load_dwordx2 v[20:21], v[6:7], off offset:2560
	global_load_dwordx2 v[104:105], v[4:5], off offset:2048
	global_load_dwordx2 v[22:23], v[4:5], off offset:2560
	s_mov_b64 s[2:3], 0
	s_waitcnt vmcnt(16)
	v_lshlrev_b32_e32 v116, 16, v76
	s_waitcnt vmcnt(15)
	v_lshlrev_b32_e32 v118, 16, v90
	v_and_b32_e32 v119, 0xffff0000, v90
	v_lshlrev_b32_e32 v90, 16, v91
	v_and_b32_e32 v91, 0xffff0000, v91
	v_and_b32_e32 v117, 0xffff0000, v76
	v_lshlrev_b32_e32 v76, 16, v77
	v_and_b32_e32 v77, 0xffff0000, v77
	s_waitcnt vmcnt(13)
	v_lshlrev_b32_e32 v122, 16, v94
	v_and_b32_e32 v123, 0xffff0000, v94
	v_lshlrev_b32_e32 v106, 16, v18
	v_lshlrev_b32_e32 v108, 16, v68
	v_lshlrev_b32_e32 v112, 16, v70
	v_and_b32_e32 v113, 0xffff0000, v70
	v_lshlrev_b32_e32 v114, 16, v71
	v_and_b32_e32 v115, 0xffff0000, v71
	v_lshlrev_b32_e32 v70, 16, v74
	v_and_b32_e32 v71, 0xffff0000, v74
	v_lshlrev_b32_e32 v74, 16, v75
	v_and_b32_e32 v75, 0xffff0000, v75
	v_and_b32_e32 v109, 0xffff0000, v68
	v_lshlrev_b32_e32 v110, 16, v69
	v_and_b32_e32 v111, 0xffff0000, v69
	v_lshlrev_b32_e32 v68, 16, v72
	v_and_b32_e32 v69, 0xffff0000, v72
	v_lshlrev_b32_e32 v72, 16, v73
	v_and_b32_e32 v73, 0xffff0000, v73
	v_pk_mul_f32 v[70:71], v[66:67], v[70:71] op_sel_hi:[0,1]
	v_pk_mul_f32 v[74:75], v[66:67], v[74:75] op_sel_hi:[0,1]
	v_and_b32_e32 v107, 0xffff0000, v18
	v_lshlrev_b32_e32 v18, 16, v19
	v_and_b32_e32 v19, 0xffff0000, v19
	v_pk_mul_f32 v[118:119], v[66:67], v[118:119] op_sel_hi:[0,1]
	v_pk_mul_f32 v[90:91], v[66:67], v[90:91] op_sel_hi:[0,1]
	v_pk_fma_f32 v[68:69], v[64:65], v[68:69], v[70:71] op_sel_hi:[0,1,1]
	v_pk_fma_f32 v[72:73], v[64:65], v[72:73], v[74:75] op_sel_hi:[0,1,1]
	v_lshlrev_b32_e32 v120, 16, v92
	v_and_b32_e32 v121, 0xffff0000, v92
	v_lshlrev_b32_e32 v94, 16, v95
	v_and_b32_e32 v95, 0xffff0000, v95
	v_pk_mul_f32 v[122:123], v[66:67], v[122:123] op_sel_hi:[0,1]
	v_pk_fma_f32 v[74:75], v[64:65], v[116:117], v[118:119] op_sel_hi:[0,1,1]
	v_pk_fma_f32 v[76:77], v[64:65], v[76:77], v[90:91] op_sel_hi:[0,1,1]
	s_waitcnt vmcnt(12)
	v_pk_fma_f32 v[70:71], v[8:9], v[68:69], v[106:107]
	v_pk_fma_f32 v[68:69], v[10:11], v[72:73], v[18:19]
	v_lshlrev_b32_e32 v92, 16, v93
	v_and_b32_e32 v93, 0xffff0000, v93
	v_pk_mul_f32 v[94:95], v[66:67], v[94:95] op_sel_hi:[0,1]
	v_pk_fma_f32 v[90:91], v[64:65], v[120:121], v[122:123] op_sel_hi:[0,1,1]
	s_waitcnt vmcnt(11)
	v_pk_fma_f32 v[74:75], v[12:13], v[74:75], v[108:109]
	v_pk_fma_f32 v[72:73], v[14:15], v[76:77], v[110:111]
	v_pk_mul_f32 v[12:13], v[68:69], v[68:69]
	v_pk_mul_f32 v[14:15], v[70:71], v[70:71]
	v_pk_fma_f32 v[92:93], v[64:65], v[92:93], v[94:95] op_sel_hi:[0,1,1]
	s_waitcnt vmcnt(10)
; #define GAS __attribute__((address_space(1)))
; __device__ __forceinline__ void final_phase(Frame& F) {
;     ...
;             for (int j = 0; j < 8; ++j) { const int col = 4 * (F.lane + 64 * j);
;                 const v2u ya = *(const GAS v2u*)(Y2 + s0 + col), yb = *(const GAS v2u*)(Y2 + s1 + col); const f32x4 gg = *(const GAS f32x4*)(g2 + col);
;                 f32x4 mo; mo.x = w0 * bflo(ya.x) + w1 * bflo(yb.x); mo.y = w0 * bfhi(ya.x) + w1 * bfhi(yb.x); mo.z = w0 * bflo(ya.y) + w1 * bflo(yb.y); mo.w = w0 * bfhi(ya.y) + w1 * bfhi(yb.y);
;                 { const v2u hw = hr[64 * j]; f32x4 hv; hv.x = bflo(hw.x); hv.y = bfhi(hw.x); hv.z = bflo(hw.y); hv.w = bfhi(hw.y); v[j] = hv + gg * mo; } s += (v[j].x * v[j].x + v[j].y * v[j].y) + (v[j].z * v[j].z + v[j].w * v[j].w); }
	v_pk_fma_f32 v[8:9], v[80:81], v[90:91], v[112:113]
	v_pk_mul_f32 v[18:19], v[72:73], v[72:73]
	v_pk_mul_f32 v[76:77], v[74:75], v[74:75]
	v_pk_mov_b32 v[80:81], v[14:15], v[12:13] op_sel:[1,0]
	v_mov_b32_e32 v15, v13
	global_load_dwordx2 v[94:95], v[58:59], off offset:2560
	v_pk_fma_f32 v[10:11], v[82:83], v[92:93], v[114:115]
	v_pk_mov_b32 v[12:13], v[76:77], v[18:19] op_sel:[1,0]
	v_mov_b32_e32 v77, v19
	v_pk_add_f32 v[18:19], v[80:81], v[14:15]
	s_waitcnt vmcnt(9)
	v_lshlrev_b32_e32 v14, 16, v98
	global_load_dwordx4 v[80:83], v25, s[18:19]
	v_and_b32_e32 v15, 0xffff0000, v98
	global_load_dwordx2 v[108:109], v[4:5], off offset:3072
	global_load_dwordx2 v[106:107], v[6:7], off offset:3072
	v_pk_add_f32 v[76:77], v[12:13], v[76:77]
	v_lshlrev_b32_e32 v12, 16, v96
	v_and_b32_e32 v13, 0xffff0000, v96
	v_pk_mul_f32 v[14:15], v[66:67], v[14:15] op_sel_hi:[0,1]
	v_lshlrev_b32_e32 v90, 16, v99
	v_and_b32_e32 v91, 0xffff0000, v99
	v_pk_fma_f32 v[12:13], v[64:65], v[12:13], v[14:15] op_sel_hi:[0,1,1]
	v_lshlrev_b32_e32 v14, 16, v97
	v_and_b32_e32 v15, 0xffff0000, v97
	v_pk_mul_f32 v[90:91], v[66:67], v[90:91] op_sel_hi:[0,1]
	v_pk_fma_f32 v[14:15], v[64:65], v[14:15], v[90:91] op_sel_hi:[0,1,1]
	global_load_dwordx2 v[98:99], v[58:59], off offset:3072
	s_waitcnt vmcnt(11)
	v_lshlrev_b32_e32 v90, 16, v101
	v_and_b32_e32 v91, 0xffff0000, v101
	v_lshlrev_b32_e32 v96, 16, v100
	v_and_b32_e32 v97, 0xffff0000, v100
	v_pk_fma_f32 v[14:15], v[86:87], v[14:15], v[90:91]
	global_load_dwordx4 v[90:93], v24, s[18:19]
	v_pk_fma_f32 v[12:13], v[84:85], v[12:13], v[96:97]
	v_pk_add_f32 v[18:19], v[18:19], v[18:19] op_sel:[0,1] op_sel_hi:[1,0]
	v_mul_f32_e32 v28, v12, v12
	v_mul_f32_e32 v79, v13, v13
	v_pk_add_f32 v[76:77], v[76:77], v[76:77] op_sel:[0,1] op_sel_hi:[1,0]
	v_mov_b32_e32 v19, v28
	v_mov_b32_e32 v77, v79
	v_mul_f32_e32 v28, v9, v9
	v_mul_f32_e32 v84, v14, v14
	v_pk_add_f32 v[18:19], v[18:19], v[76:77]
	v_pk_fma_f32 v[76:77], v[8:9], v[8:9], v[28:29] op_sel_hi:[1,1,0]
	v_mul_f32_e32 v28, v11, v11
	v_mul_f32_e32 v86, v15, v15
	v_mov_b32_e32 v77, v84
	v_pk_fma_f32 v[84:85], v[10:11], v[10:11], v[28:29] op_sel_hi:[1,1,0]
	global_load_dwordx2 v[96:97], v[58:59], off offset:3584
	v_mov_b32_e32 v85, v86
	v_pk_add_f32 v[76:77], v[76:77], v[84:85]
	global_load_dwordx2 v[84:85], v[6:7], off offset:3584
	global_load_dwordx2 v[86:87], v[4:5], off offset:3584
	s_waitcnt vmcnt(10)
	v_lshlrev_b32_e32 v4, 16, v104
	v_and_b32_e32 v5, 0xffff0000, v104
	v_lshlrev_b32_e32 v6, 16, v102
	v_and_b32_e32 v7, 0xffff0000, v102
	v_pk_mul_f32 v[4:5], v[66:67], v[4:5] op_sel_hi:[0,1]
	v_pk_add_f32 v[76:77], v[18:19], v[76:77]
	v_pk_fma_f32 v[18:19], v[64:65], v[6:7], v[4:5] op_sel_hi:[0,1,1]
	v_lshlrev_b32_e32 v6, 16, v105
	v_and_b32_e32 v7, 0xffff0000, v105
	v_lshlrev_b32_e32 v4, 16, v103
	v_and_b32_e32 v5, 0xffff0000, v103
	v_pk_mul_f32 v[6:7], v[66:67], v[6:7] op_sel_hi:[0,1]
	v_pk_fma_f32 v[100:101], v[64:65], v[4:5], v[6:7] op_sel_hi:[0,1,1]
	global_load_dwordx4 v[4:7], v65, s[18:19]
	v_lshlrev_b32_e32 v102, 16, v16
	v_and_b32_e32 v103, 0xffff0000, v16
	v_lshlrev_b32_e32 v104, 16, v17
	v_and_b32_e32 v105, 0xffff0000, v17
	v_pk_fma_f32 v[16:17], v[0:1], v[18:19], v[102:103]
	v_pk_fma_f32 v[18:19], v[2:3], v[100:101], v[104:105]
	v_pk_mul_f32 v[2:3], v[16:17], v[16:17]
	v_pk_mul_f32 v[0:1], v[18:19], v[18:19]
	v_pk_add_f32 v[76:77], v[76:77], v[76:77] op_sel:[0,1] op_sel_hi:[1,0]
	v_pk_mov_b32 v[100:101], v[2:3], v[0:1] op_sel:[1,0]
	v_mov_b32_e32 v3, v1
	v_pk_add_f32 v[100:101], v[100:101], v[2:3]
	s_waitcnt vmcnt(10)
	v_lshlrev_b32_e32 v2, 16, v22
	v_and_b32_e32 v3, 0xffff0000, v22
	v_lshlrev_b32_e32 v0, 16, v20
	v_and_b32_e32 v1, 0xffff0000, v20
	v_pk_mul_f32 v[2:3], v[66:67], v[2:3] op_sel_hi:[0,1]
	v_pk_fma_f32 v[0:1], v[64:65], v[0:1], v[2:3] op_sel_hi:[0,1,1]
	v_lshlrev_b32_e32 v2, 16, v21
	v_and_b32_e32 v3, 0xffff0000, v21
	v_lshlrev_b32_e32 v20, 16, v23
	v_and_b32_e32 v21, 0xffff0000, v23
	v_pk_mul_f32 v[20:21], v[66:67], v[20:21] op_sel_hi:[0,1]
	v_pk_fma_f32 v[2:3], v[64:65], v[2:3], v[20:21] op_sel_hi:[0,1,1]
	s_waitcnt vmcnt(9)
	v_lshlrev_b32_e32 v22, 16, v95
	v_and_b32_e32 v23, 0xffff0000, v95
	v_lshlrev_b32_e32 v20, 16, v94
	v_and_b32_e32 v21, 0xffff0000, v94
	s_waitcnt vmcnt(8)
	v_pk_fma_f32 v[22:23], v[82:83], v[2:3], v[22:23]
	s_waitcnt vmcnt(7)
	v_lshlrev_b32_e32 v2, 16, v108
	v_and_b32_e32 v3, 0xffff0000, v108
	v_pk_fma_f32 v[20:21], v[80:81], v[0:1], v[20:21]
	s_waitcnt vmcnt(6)
	v_lshlrev_b32_e32 v0, 16, v106
	v_and_b32_e32 v1, 0xffff0000, v106
	v_pk_mul_f32 v[2:3], v[66:67], v[2:3] op_sel_hi:[0,1]
	v_lshlrev_b32_e32 v80, 16, v109
	v_and_b32_e32 v81, 0xffff0000, v109
	v_pk_fma_f32 v[0:1], v[64:65], v[0:1], v[2:3] op_sel_hi:[0,1,1]
	v_lshlrev_b32_e32 v2, 16, v107
	v_and_b32_e32 v3, 0xffff0000, v107
	v_pk_mul_f32 v[80:81], v[66:67], v[80:81] op_sel_hi:[0,1]
	v_pk_fma_f32 v[2:3], v[64:65], v[2:3], v[80:81] op_sel_hi:[0,1,1]
	s_waitcnt vmcnt(5)
	v_lshlrev_b32_e32 v80, 16, v98
	v_and_b32_e32 v81, 0xffff0000, v98
	v_lshlrev_b32_e32 v82, 16, v99
	s_waitcnt vmcnt(4)
	v_pk_fma_f32 v[0:1], v[90:91], v[0:1], v[80:81]
	v_and_b32_e32 v83, 0xffff0000, v99
	v_mul_f32_e32 v28, v0, v0
	v_mul_f32_e32 v79, v1, v1
	v_pk_add_f32 v[80:81], v[100:101], v[100:101] op_sel:[0,1] op_sel_hi:[1,0]
	v_pk_fma_f32 v[2:3], v[92:93], v[2:3], v[82:83]
	v_mov_b32_e32 v77, v28
	v_mov_b32_e32 v81, v79
	v_mul_f32_e32 v28, v21, v21
	v_mul_f32_e32 v82, v2, v2
	v_pk_add_f32 v[76:77], v[76:77], v[80:81]
	v_pk_fma_f32 v[80:81], v[20:21], v[20:21], v[28:29] op_sel_hi:[1,1,0]
	v_mul_f32_e32 v28, v23, v23
	v_mul_f32_e32 v89, v3, v3
	v_mov_b32_e32 v81, v82
	v_pk_fma_f32 v[82:83], v[22:23], v[22:23], v[28:29] op_sel_hi:[1,1,0]
	s_nop 0
	v_mov_b32_e32 v83, v89
	v_pk_add_f32 v[80:81], v[80:81], v[82:83]
	s_waitcnt vmcnt(1)
	v_lshlrev_b32_e32 v82, 16, v87
	v_pk_add_f32 v[76:77], v[76:77], v[80:81]
	v_lshlrev_b32_e32 v80, 16, v86
	v_and_b32_e32 v81, 0xffff0000, v86
	v_add_f32_e32 v28, v76, v77
	v_lshlrev_b32_e32 v76, 16, v84
	v_and_b32_e32 v77, 0xffff0000, v84
	v_pk_mul_f32 v[80:81], v[66:67], v[80:81] op_sel_hi:[0,1]
	v_and_b32_e32 v83, 0xffff0000, v87
	v_pk_fma_f32 v[76:77], v[64:65], v[76:77], v[80:81] op_sel_hi:[0,1,1]
	v_lshlrev_b32_e32 v80, 16, v85
	v_and_b32_e32 v81, 0xffff0000, v85
	v_pk_mul_f32 v[82:83], v[66:67], v[82:83] op_sel_hi:[0,1]
	v_pk_fma_f32 v[80:81], v[64:65], v[80:81], v[82:83] op_sel_hi:[0,1,1]
	v_lshlrev_b32_e32 v82, 16, v96
	v_and_b32_e32 v83, 0xffff0000, v96
	v_lshlrev_b32_e32 v84, 16, v97
	v_and_b32_e32 v85, 0xffff0000, v97
	s_waitcnt vmcnt(0)
	v_pk_fma_f32 v[6:7], v[6:7], v[80:81], v[84:85]
	v_pk_fma_f32 v[4:5], v[4:5], v[76:77], v[82:83]
